# phase 5 tail: scan waves (0-3) run at raised issue priority over the weight-conversion waves sharing their SIMDs
# speedup vs baseline: 1.0129x; 1.0129x over previous
.LBB0_911:
	s_or_b64 exec, exec, s[0:1]
	s_setprio 0
	v_readlane_b32 s0, v253, 21
	v_readlane_b32 s1, v253, 22
	s_andn2_b64 vcc, exec, s[0:1]
	s_barrier
	s_cbranch_vccnz .LBB0_1005
	v_readlane_b32 s12, v251, 36
	s_cmp_gt_u32 s12, 3
	s_cbranch_scc1 .Lprio_h2
	s_setprio 3
.Lprio_h2:
	v_readlane_b32 s12, v254, 51
	s_add_i32 s80, s12, 1
	s_cmp_lg_u32 s12, 3
	s_cselect_b64 s[56:57], -1, 0
	s_lshl_b64 s[0:1], s[80:81], 14
	s_lshl_b64 s[2:3], s[80:81], 17
	s_bitcmp1_b32 s80, 0
	s_mov_b64 s[30:31], s[76:77]
	v_readlane_b32 s36, v251, 20
	s_cselect_b32 s29, s85, 0x713d000
	s_cselect_b32 s27, 0x66f0000, 0
	s_lshl_b64 s[34:35], s[80:81], 16
	s_lshl_b64 s[52:53], s[80:81], 18
	s_lshl_b64 s[54:55], s[80:81], 22
	s_lshl_b64 s[90:91], s[80:81], 26
	s_lshl_b32 s85, s12, 8
	s_lshl_b32 s31, s12, 6
	v_readlane_b32 s50, v251, 34
	v_readlane_b32 s37, v251, 21
	v_readlane_b32 s51, v251, 35
	s_add_u32 s36, s50, s0
	s_addc_u32 s37, s51, s1
	s_add_u32 s76, s62, s2
	s_addc_u32 s77, s63, s3
	s_add_u32 s0, s74, s27
	v_readlane_b32 s12, v251, 39
	s_addc_u32 s1, s75, 0
	v_readlane_b32 s24, v251, 51
	v_readlane_b32 s25, v251, 52
	s_add_u32 s2, s24, s34
	s_addc_u32 s3, s25, s35
	v_readlane_b32 s18, v251, 45
	v_writelane_b32 v255, s3, 0
	s_add_u32 s3, s0, 0x1135000
	v_writelane_b32 v255, s3, 1
	s_addc_u32 s3, s1, 0
	v_readlane_b32 s19, v251, 46
	v_writelane_b32 v255, s3, 2
	s_add_u32 s3, s18, s52
	v_writelane_b32 v255, s3, 3
	s_addc_u32 s3, s19, s53
	v_writelane_b32 v255, s3, 4
	s_mov_b32 s19, s2
	s_add_u32 s2, s0, 0x1115000
	s_mul_i32 s28, s80, 0x48000
	v_readlane_b32 s14, v251, 41
	v_writelane_b32 v255, s2, 5
	s_addc_u32 s2, s1, 0
	v_writelane_b32 v255, s2, 6
	s_add_u32 s2, s14, s28
	v_readlane_b32 s15, v251, 42
	v_writelane_b32 v255, s2, 7
	s_mul_hi_u32 s2, s80, 0x48000
	s_addc_u32 s2, s15, s2
	v_writelane_b32 v255, s2, 8
	s_add_u32 s2, s0, 0x10f1000
	v_readlane_b32 s48, v251, 32
	v_writelane_b32 v255, s2, 9
	s_addc_u32 s2, s1, 0
	v_readlane_b32 s49, v251, 33
	v_writelane_b32 v255, s2, 10
	s_add_u32 s2, s48, s54
	v_readlane_b32 s40, v251, 24
	v_readlane_b32 s41, v251, 25
	v_readlane_b32 s42, v251, 26
	v_readlane_b32 s43, v251, 27
	v_readlane_b32 s44, v251, 28
	v_readlane_b32 s45, v251, 29
	v_readlane_b32 s46, v251, 30
	v_readlane_b32 s47, v251, 31
	v_writelane_b32 v255, s2, 11
	s_addc_u32 s2, s49, s55
	v_writelane_b32 v255, s2, 12
	s_add_u32 s3, s0, 0xef1000
	v_readlane_b32 s40, v251, 4
	s_mul_i32 s2, s80, 0x860000
	v_writelane_b32 v255, s3, 13
	s_addc_u32 s3, s1, 0
	v_readlane_b32 s54, v251, 18
	v_writelane_b32 v255, s3, 14
	s_add_u32 s2, s54, s2
	v_readlane_b32 s55, v251, 19
	v_writelane_b32 v255, s2, 15
	s_mul_hi_u32 s2, s80, 0x860000
	s_addc_u32 s2, s55, s2
	v_writelane_b32 v255, s2, 16
	s_add_u32 s2, s0, 0xa71000
	v_readlane_b32 s20, v251, 47
	v_writelane_b32 v255, s2, 17
	s_addc_u32 s2, s1, 0
	v_readlane_b32 s21, v251, 48
	s_add_u32 s20, s70, s90
	s_addc_u32 s21, s71, s91
	v_readlane_b32 s13, v251, 40
	s_add_u32 s12, s0, 0x513d000
	s_addc_u32 s13, s1, 0
	s_add_u32 s82, s0, 0x113d000
	s_addc_u32 s88, s1, 0
	s_add_u32 s0, s74, s29
	v_writelane_b32 v255, s2, 18
	s_addc_u32 s1, s75, 0
	v_readlane_b32 s16, v251, 43
	v_readlane_b32 s17, v251, 44
	v_writelane_b32 v255, s0, 19
	s_mov_b64 s[16:17], s[56:57]
	s_mov_b32 s18, s31
	v_writelane_b32 v255, s1, 20
	v_readlane_b32 s89, v254, 19
	s_mov_b32 s2, s30
	v_readlane_b32 s38, v251, 22
	v_readlane_b32 s39, v251, 23
	v_readlane_b32 s22, v251, 49
	v_readlane_b32 s23, v251, 50
	v_readlane_b32 s26, v251, 53
	v_readlane_b32 s27, v251, 54
	v_readlane_b32 s41, v251, 5
	v_readlane_b32 s42, v251, 6
	v_readlane_b32 s43, v251, 7
	v_readlane_b32 s44, v251, 8
	v_readlane_b32 s45, v251, 9
	v_readlane_b32 s46, v251, 10
	v_readlane_b32 s47, v251, 11
	v_readlane_b32 s48, v251, 12
	v_readlane_b32 s49, v251, 13
	v_readlane_b32 s50, v251, 14
	v_readlane_b32 s51, v251, 15
	v_readlane_b32 s52, v251, 16
	v_readlane_b32 s53, v251, 17
	s_branch .LBB0_914

.LBB0_1005:
	s_setprio 0
	v_readlane_b32 s0, v254, 63
	s_add_i32 s2, s0, 4
	v_readlane_b32 s0, v251, 37
	v_readlane_b32 s1, v251, 38
	s_cmp_ge_i32 s2, s1
	s_cbranch_scc1 .LBB0_1055
	s_waitcnt vmcnt(0)
	s_barrier
	s_mov_b64 s[0:1], exec
	v_readlane_b32 s12, v251, 2
	v_readlane_b32 s13, v251, 3
	s_and_b64 s[12:13], s[0:1], s[12:13]
	s_mov_b64 exec, s[12:13]
	s_cbranch_execz .LBB0_1054
	v_readlane_b32 s3, v254, 24
	s_waitcnt vmcnt(0) expcnt(0) lgkmcnt(0)
	s_nop 0
	v_mov_b32_e32 v1, s3
	ds_read_b32 v3, v1
	v_readlane_b32 s3, v254, 25
	s_waitcnt lgkmcnt(0)
	v_cmp_ne_u32_e32 vcc, 0, v3
	v_mov_b32_e32 v1, s3
	ds_read_b32 v2, v1
	s_cbranch_vccnz .LBB0_1022
	v_readlane_b32 s14, v251, 0
	v_readlane_b32 s15, v251, 1
	s_load_dwordx2 s[12:13], s[14:15], 0x4
	s_mov_b32 s18, 1
	s_waitcnt lgkmcnt(0)
	s_mul_i32 s3, s12, s94
	s_mul_i32 s3, s3, s13
	s_branch .LBB0_1010
